# P1 tile loop: S1 drain only on loop entry; P15: next-unit gather offsets formed at the start of the load part instead of between the closing wait and the barrier
# baseline (speedup 1.0000x reference)
.LBB0_218:
	s_andn2_b64 vcc, exec, s[4:5]
	s_cbranch_vccnz .LBB0_601
	v_writelane_b32 v254, s97, 18
	s_add_u32 s0, s72, 0x10000
	v_writelane_b32 v254, s0, 10
	s_addc_u32 s86, s73, 0
	v_readlane_b32 s4, v254, 6
	s_mov_b32 s9, 0
	v_readlane_b32 s5, v254, 7
	s_add_u32 s38, s72, 0xdd00000
	s_mov_b32 s5, s9
	s_addc_u32 s39, s73, 0
	s_add_i32 s6, s4, 32
	v_mov_b32_e32 v8, 0
	s_lshl_b32 s92, s4, 7
	s_lshl_b64 s[0:1], s[4:5], 16
	v_lshlrev_b32_e32 v4, 3, v0
	v_mov_b32_e32 v5, v8
	s_add_u32 s0, s72, s0
	v_lshl_add_u64 v[6:7], s[48:49], 0, v[4:5]
	s_addc_u32 s1, s73, s1
	v_lshlrev_b32_e32 v4, 4, v250
	v_lshl_add_u64 v[4:5], s[0:1], 0, v[4:5]
	s_mov_b64 s[0:1], 0x1900000
	v_lshl_add_u64 v[172:173], v[4:5], 0, s[0:1]
	s_lshl_b32 s0, s4, 4
	s_and_b32 s77, s0, 0xfffffe0
	s_lshl_b32 s0, s4, 8
	s_mul_i32 s5, s4, 0x810
	s_add_i32 s93, s0, 0
	s_add_i32 s0, s5, 0x4080
	v_writelane_b32 v254, s0, 19
	s_add_i32 s0, s5, 0x8100
	v_writelane_b32 v254, s0, 20
	s_add_i32 s0, s5, 0xc180
	v_writelane_b32 v254, s0, 21
	s_add_i32 s93, s93, 0x20600
	s_add_i32 s95, s4, 8
	s_add_i32 s97, s4, 16
	s_add_i32 s35, s4, 24
	v_readlane_b32 s1, v254, 5
	s_cmpk_lt_u32 s1, 0x800
	s_cselect_b64 s[42:43], -1, 0
	s_min_u32 s0, s6, 63
	v_writelane_b32 v254, s6, 12
	s_lshl_b32 s6, s0, 12
	s_mov_b32 s7, s9
	v_writelane_b32 v254, s6, 22
	s_add_i32 s0, s4, 40
	s_cmpk_lt_u32 s1, 0x600
	v_writelane_b32 v254, s7, 23
	s_cselect_b64 s[46:47], -1, 0
	v_writelane_b32 v254, s0, 24
	s_min_u32 s0, s0, 63
	s_lshl_b32 s6, s0, 12
	s_mov_b32 s7, s9
	v_writelane_b32 v254, s6, 25
	s_add_i32 s0, s4, 48
	s_cmpk_lt_u32 s1, 0x400
	v_writelane_b32 v254, s7, 26
	s_cselect_b64 s[56:57], -1, 0
	v_writelane_b32 v254, s0, 27
	s_min_u32 s0, s0, 63
	s_lshl_b32 s6, s0, 12
	s_mov_b32 s7, s9
	v_writelane_b32 v254, s6, 28
	s_mov_b32 s0, s4
	v_lshlrev_b32_e32 v2, 1, v0
	v_writelane_b32 v254, s7, 29
	v_writelane_b32 v254, s0, 6
	v_mov_b32_e32 v10, v8
	v_mov_b32_e32 v11, v8
	v_writelane_b32 v254, s1, 7
	s_add_i32 s0, s4, 56
	s_cmpk_lt_u32 s1, 0x200
	s_cselect_b64 s[60:61], -1, 0
	v_writelane_b32 v254, s0, 30
	s_min_u32 s0, s0, 63
	s_lshl_b32 s0, s0, 12
	s_mov_b32 s1, s9
	v_writelane_b32 v254, s0, 31
	v_mov_b32_e32 v12, v8
	v_mov_b32_e32 v13, v8
	v_mov_b32_e32 v14, v8
	v_mov_b32_e32 v15, v8
	v_mov_b32_e32 v16, v8
	v_mov_b32_e32 v17, v8
	v_mov_b32_e32 v18, v8
	v_mov_b32_e32 v19, v8
	v_mov_b32_e32 v20, v8
	v_mov_b32_e32 v21, v8
	v_mov_b32_e32 v22, v8
	v_mov_b32_e32 v23, v8
	v_mov_b32_e32 v24, v8
	v_mov_b32_e32 v25, v8
	v_mov_b32_e32 v26, v8
	v_mov_b32_e32 v27, v8
	v_mov_b32_e32 v28, v8
	v_mov_b32_e32 v29, v8
	v_mov_b32_e32 v30, v8
	v_mov_b32_e32 v31, v8
	v_and_b32_e32 v1, 15, v0
	v_lshl_add_u32 v211, v0, 2, 0
	v_writelane_b32 v254, s1, 32
	v_mov_b32_e32 v9, v8
	v_lshlrev_b32_e32 v174, 2, v2
	v_mbcnt_lo_u32_b32 v2, -1, 0
	v_mov_b64_e32 v[40:41], v[30:31]
	v_lshrrev_b32_e32 v171, 4, v250
	v_lshl_add_u32 v210, v250, 3, 0
	v_add_u32_e32 v212, 0xffffa750, v211
	v_add_u32_e32 v213, 0xffffb770, v211
	v_add_u32_e32 v214, 0xffff8710, v211
	v_add_u32_e32 v215, 0xffffbf80, v211
	v_writelane_b32 v254, s5, 14
	s_add_i32 s0, s5, 0x10200
	v_mov_b32_e32 v216, 0x358637bd
	s_mov_b32 s88, 0x800000
	v_mbcnt_hi_u32_b32 v217, -1, v2
	v_mov_b64_e32 v[38:39], v[28:29]
	v_mov_b64_e32 v[36:37], v[26:27]
	v_mov_b64_e32 v[34:35], v[24:25]
	v_mov_b64_e32 v[32:33], v[22:23]
	v_mov_b64_e32 v[30:31], v[20:21]
	v_mov_b64_e32 v[28:29], v[18:19]
	v_mov_b64_e32 v[26:27], v[16:17]
	v_mov_b64_e32 v[24:25], v[14:15]
	v_mov_b64_e32 v[22:23], v[12:13]
	v_mov_b64_e32 v[20:21], v[10:11]
	v_mov_b64_e32 v[18:19], v[8:9]
	v_mov_b64_e32 v[16:17], v[6:7]
	v_mov_b64_e32 v[14:15], v[4:5]
	v_mov_b64_e32 v[12:13], v[2:3]
	s_mov_b32 s18, 0
	v_writelane_b32 v254, s0, 33
	v_mov_b64_e32 v[10:11], v[0:1]
	s_waitcnt vmcnt(0)
	s_branch .LBB0_221

.LBB0_230:
	v_mul_f32_e32 v11, v51, v51
	v_mul_f32_e32 v17, v53, v53
	v_fmac_f32_e32 v11, v50, v50
	v_fmac_f32_e32 v17, v52, v52
	v_add_f32_e32 v11, v11, v17
	v_mul_f32_e32 v17, v47, v47
	v_mul_f32_e32 v110, v49, v49
	v_fmac_f32_e32 v17, v46, v46
	v_fmac_f32_e32 v110, v48, v48
	v_add_f32_e32 v17, v17, v110
	v_add_f32_e32 v11, v11, v17
	v_mul_f32_e32 v17, v63, v63
	v_mul_f32_e32 v110, v65, v65
	v_fmac_f32_e32 v17, v62, v62
	v_fmac_f32_e32 v110, v64, v64
	v_and_b32_e32 v9, 64, v217
	v_add_f32_e32 v17, v17, v110
	v_add_u32_e32 v10, 64, v9
	v_xor_b32_e32 v9, 1, v217
	v_add_f32_e32 v11, v11, v17
	v_mul_f32_e32 v17, v55, v55
	v_mul_f32_e32 v110, v57, v57
	v_cmp_lt_i32_e32 vcc, v9, v10
	v_fmac_f32_e32 v17, v54, v54
	v_fmac_f32_e32 v110, v56, v56
	v_cndmask_b32_e32 v9, v217, v9, vcc
	v_add_f32_e32 v17, v17, v110
	v_lshlrev_b32_e32 v9, 2, v9
	v_add_f32_e32 v11, v11, v17
	ds_bpermute_b32 v110, v9, v11
	v_xor_b32_e32 v17, 2, v217
	v_cmp_lt_i32_e32 vcc, v17, v10
	v_xor_b32_e32 v113, 16, v217
	v_readlane_b32 s0, v254, 6
	v_cndmask_b32_e32 v17, v217, v17, vcc
	v_lshlrev_b32_e32 v17, 2, v17
	s_waitcnt lgkmcnt(0)
	v_add_f32_e32 v11, v11, v110
	ds_bpermute_b32 v111, v17, v11
	v_xor_b32_e32 v110, 4, v217
	v_cmp_lt_i32_e32 vcc, v110, v10
	s_cmp_ge_u32 s0, s8
	s_waitcnt lgkmcnt(0)
	v_cndmask_b32_e32 v110, v217, v110, vcc
	v_lshlrev_b32_e32 v110, 2, v110
	v_add_f32_e32 v11, v11, v111
	ds_bpermute_b32 v112, v110, v11
	v_xor_b32_e32 v111, 8, v217
	v_cmp_lt_i32_e32 vcc, v111, v10
	s_barrier
	v_readlane_b32 s1, v254, 7
	v_cndmask_b32_e32 v111, v217, v111, vcc
	v_lshlrev_b32_e32 v111, 2, v111
	s_waitcnt lgkmcnt(0)
	v_add_f32_e32 v11, v11, v112
	ds_bpermute_b32 v112, v111, v11
	v_cmp_lt_i32_e32 vcc, v113, v10
	s_waitcnt lgkmcnt(0)
	v_add_f32_e32 v11, v11, v112
	v_cndmask_b32_e32 v113, v217, v113, vcc
	v_lshlrev_b32_e32 v219, 2, v113
	ds_bpermute_b32 v112, v219, v11
	v_xor_b32_e32 v113, 32, v217
	v_cmp_lt_i32_e32 vcc, v113, v10
	s_nop 1
	v_cndmask_b32_e32 v10, v217, v113, vcc
	v_lshlrev_b32_e32 v220, 2, v10
	s_waitcnt lgkmcnt(0)
	v_add_f32_e32 v10, v11, v112
	ds_bpermute_b32 v11, v220, v10
	s_cbranch_scc1 .LBB0_232
	s_waitcnt lgkmcnt(0)
	v_add_f32_e32 v10, v10, v11
	v_fmamk_f32 v10, v10, 0x3a800000, v216
	v_mul_f32_e32 v11, 0x4b800000, v10
	v_cmp_gt_f32_e32 vcc, s88, v10
	v_readlane_b32 s0, v254, 14
	s_nop 0
	v_cndmask_b32_e32 v10, v10, v11, vcc
	v_rsq_f32_e32 v10, v10
	s_nop 0
	v_mul_f32_e32 v11, 0x45800000, v10
	v_cndmask_b32_e32 v10, v10, v11, vcc
	v_pk_mul_f32 v[52:53], v[52:53], v[10:11] op_sel_hi:[1,0]
	v_pk_mul_f32 v[50:51], v[50:51], v[10:11] op_sel_hi:[1,0]
	v_pk_mul_f32 v[46:47], v[46:47], v[10:11] op_sel_hi:[1,0]
	v_cvt_pk_bf16_f32 v50, v50, v51
	v_cvt_pk_bf16_f32 v51, v52, v53
	v_add_u32_e32 v52, s0, v210
	ds_write_b64 v52, v[50:51]
	v_pk_mul_f32 v[48:49], v[48:49], v[10:11] op_sel_hi:[1,0]
	v_cvt_pk_bf16_f32 v46, v46, v47
	s_nop 0
	v_cvt_pk_bf16_f32 v47, v48, v49
	ds_write_b64 v52, v[46:47] offset:512
	v_pk_mul_f32 v[46:47], v[64:65], v[10:11] op_sel_hi:[1,0]
	v_pk_mul_f32 v[48:49], v[62:63], v[10:11] op_sel_hi:[1,0]
	s_nop 0
	v_cvt_pk_bf16_f32 v48, v48, v49
	v_cvt_pk_bf16_f32 v49, v46, v47
	v_pk_mul_f32 v[46:47], v[56:57], v[10:11] op_sel_hi:[1,0]
	v_pk_mul_f32 v[10:11], v[54:55], v[10:11] op_sel_hi:[1,0]
	ds_write_b64 v52, v[48:49] offset:1024
	v_cvt_pk_bf16_f32 v10, v10, v11
	v_cvt_pk_bf16_f32 v11, v46, v47
	ds_write_b64 v52, v[10:11] offset:1536

.LBB0_1911:
	ds_read_b128 v[18:21], v197
	ds_read_b128 v[22:25], v197 offset:1024
	ds_read_b128 v[26:29], v197 offset:2048
	ds_read_b128 v[30:33], v197 offset:3072
	ds_read_b128 v[2:5], v198
	ds_read_b128 v[6:9], v198 offset:1024
	ds_read_b128 v[10:13], v198 offset:2048
	ds_read_b128 v[14:17], v198 offset:3072
	s_add_u32 s42, s46, 0x100
	s_addc_u32 s43, s47, 0
	s_add_u32 s48, s37, s46
	s_addc_u32 s49, s80, s47
	s_cmpk_eq_i32 s46, 0x300
	s_cselect_b64 vcc, -1, 0
	s_and_b64 s[44:45], vcc, exec
	s_cselect_b32 s81, 0, s42
	s_cselect_b32 s76, 0, s43
	s_cselect_b32 s44, s38, s48
	s_cselect_b32 s45, s39, s49
	s_add_u32 s48, s8, s81
	s_addc_u32 s49, s9, s76
	v_lshl_add_u64 v[228:229], v[180:181], 0, s[46:47]
	s_add_i32 m0, s41, 0xc000
	ds_read_b128 v[184:187], v199
	ds_read_b128 v[188:191], v199 offset:1024
	ds_read_b128 v[204:207], v199 offset:2048
	ds_read_b128 v[208:211], v199 offset:3072
	ds_read_b128 v[212:215], v199 offset:4096
	ds_read_b128 v[216:219], v199 offset:5120
	ds_read_b128 v[220:223], v199 offset:6144
	ds_read_b128 v[224:227], v199 offset:7168
	global_load_lds_dwordx4 v[228:229], off
	v_lshl_add_u64 v[228:229], v[182:183], 0, s[46:47]
	s_add_i32 m0, s41, 0xe000
	s_nop 0
	global_load_lds_dwordx4 v[228:229], off
	s_waitcnt vmcnt(8)
	s_waitcnt lgkmcnt(0)
	s_barrier
	s_setprio 1
	s_waitcnt lgkmcnt(0)
	v_mfma_f32_16x16x128_f8f6f4 v[158:161], v[18:25], v[184:191], v[158:161]
	v_mfma_f32_16x16x128_f8f6f4 v[150:153], v[26:33], v[184:191], v[150:153]
	v_mfma_f32_16x16x128_f8f6f4 v[142:145], v[18:25], v[204:211], v[142:145]
	v_mfma_f32_16x16x128_f8f6f4 v[134:137], v[26:33], v[204:211], v[134:137]
	v_mfma_f32_16x16x128_f8f6f4 v[126:129], v[18:25], v[212:219], v[126:129]
	v_mfma_f32_16x16x128_f8f6f4 v[118:121], v[26:33], v[212:219], v[118:121]
	v_mfma_f32_16x16x128_f8f6f4 v[110:113], v[18:25], v[220:227], v[110:113]
	v_mfma_f32_16x16x128_f8f6f4 v[102:105], v[26:33], v[220:227], v[102:105]
	s_setprio 0
	s_setprio 1
	v_mfma_f32_16x16x128_f8f6f4 v[154:157], v[2:9], v[184:191], v[154:157]
	v_mfma_f32_16x16x128_f8f6f4 v[146:149], v[10:17], v[184:191], v[146:149]
	v_mfma_f32_16x16x128_f8f6f4 v[138:141], v[2:9], v[204:211], v[138:141]
	v_mfma_f32_16x16x128_f8f6f4 v[130:133], v[10:17], v[204:211], v[130:133]
	v_mfma_f32_16x16x128_f8f6f4 v[122:125], v[2:9], v[212:219], v[122:125]
	v_mfma_f32_16x16x128_f8f6f4 v[114:117], v[10:17], v[212:219], v[114:117]
	v_mfma_f32_16x16x128_f8f6f4 v[106:109], v[2:9], v[220:227], v[106:109]
	v_mfma_f32_16x16x128_f8f6f4 v[98:101], v[10:17], v[220:227], v[98:101]
	s_setprio 0
	s_barrier
	v_lshl_or_b32 v179, v236, 10, v194
	v_lshl_or_b32 v175, v237, 10, v194
	v_lshl_or_b32 v201, v238, 10, v194
	v_lshl_or_b32 v200, v239, 10, v194
	s_add_i32 s46, s5, s52
	s_mov_b64 s[98:99], s[44:45]
	s_mov_b32 m0, s46
	ds_read_b128 v[204:207], v199 offset:16384
	ds_read_b128 v[208:211], v199 offset:17408
	ds_read_b128 v[212:215], v199 offset:18432
	ds_read_b128 v[216:219], v199 offset:19456
	ds_read_b128 v[220:223], v199 offset:20480
	ds_read_b128 v[224:227], v199 offset:21504
	ds_read_b128 v[228:231], v199 offset:22528
	ds_read_b128 v[232:235], v199 offset:23552
	global_load_lds_dwordx4 v164, s[98:99]
	s_add_i32 m0, s46, 0x2000
	s_add_u32 s46, s44, 0x20000
	s_addc_u32 s47, s45, 0
	s_add_i32 s76, s66, s52
	global_load_lds_dwordx4 v166, s[98:99]
	s_mov_b32 m0, s76
	v_cndmask_b32_e32 v168, v202, v179, vcc
	global_load_lds_dwordx4 v164, s[46:47]
	v_lshl_add_u64 v[188:189], s[46:47], 0, v[166:167]
	s_add_i32 m0, s76, 0x2000
	v_lshl_add_u64 v[190:191], s[48:49], 0, v[168:169]
	global_load_lds_dwordx4 v166, s[46:47]
	s_mov_b32 m0, s41
	v_cndmask_b32_e32 v188, v176, v201, vcc
	global_load_lds_dwordx4 v168, s[48:49]
	s_mov_b32 m0, s53
	v_mov_b32_e32 v189, v169
	global_load_lds_dwordx4 v188, s[48:49]
	s_waitcnt vmcnt(8)
	s_waitcnt lgkmcnt(0)
	v_lshl_add_u64 v[188:189], s[48:49], 0, v[188:189]
	s_barrier
	s_setprio 1
	s_waitcnt lgkmcnt(0)
	v_mfma_f32_16x16x128_f8f6f4 v[94:97], v[18:25], v[204:211], v[94:97]
	v_mfma_f32_16x16x128_f8f6f4 v[86:89], v[26:33], v[204:211], v[86:89]
	v_mfma_f32_16x16x128_f8f6f4 v[78:81], v[18:25], v[212:219], v[78:81]
	v_mfma_f32_16x16x128_f8f6f4 v[70:73], v[26:33], v[212:219], v[70:73]
	v_mfma_f32_16x16x128_f8f6f4 v[58:61], v[18:25], v[220:227], v[58:61]
	v_mfma_f32_16x16x128_f8f6f4 v[46:49], v[26:33], v[220:227], v[46:49]
	v_mfma_f32_16x16x128_f8f6f4 v[38:41], v[18:25], v[228:235], v[38:41]
	v_mfma_f32_16x16x128_f8f6f4 v[34:37], v[26:33], v[228:235], v[34:37]
	s_setprio 0
	s_setprio 1
	v_mfma_f32_16x16x128_f8f6f4 v[90:93], v[2:9], v[204:211], v[90:93]
	v_mfma_f32_16x16x128_f8f6f4 v[82:85], v[10:17], v[204:211], v[82:85]
	v_mfma_f32_16x16x128_f8f6f4 v[74:77], v[2:9], v[212:219], v[74:77]
	v_mfma_f32_16x16x128_f8f6f4 v[66:69], v[10:17], v[212:219], v[66:69]
	v_mfma_f32_16x16x128_f8f6f4 v[50:53], v[2:9], v[220:227], v[50:53]
	v_mfma_f32_16x16x128_f8f6f4 v[42:45], v[10:17], v[220:227], v[42:45]
	v_mfma_f32_16x16x128_f8f6f4 v[62:65], v[2:9], v[228:235], v[62:65]
	v_mfma_f32_16x16x128_f8f6f4 v[54:57], v[10:17], v[228:235], v[54:57]
	s_setprio 0
	s_barrier
	s_add_i32 s46, 0, 0x18000
	s_add_i32 s47, 0, 0x1c000
	v_add_u32_e32 v14, s46, v177
	v_add_u32_e32 v30, s47, v177
	ds_read_b128 v[2:5], v14
	ds_read_b128 v[6:9], v14 offset:1024
	ds_read_b128 v[10:13], v14 offset:2048
	ds_read_b128 v[14:17], v14 offset:3072
	ds_read_b128 v[18:21], v30
	ds_read_b128 v[22:25], v30 offset:1024
	ds_read_b128 v[26:29], v30 offset:2048
	ds_read_b128 v[30:33], v30 offset:3072
	s_mov_b32 m0, s59
	v_cndmask_b32_e32 v168, v174, v175, vcc
	ds_read_b128 v[204:207], v199 offset:32768
	ds_read_b128 v[208:211], v199 offset:33792
	ds_read_b128 v[212:215], v199 offset:34816
	ds_read_b128 v[216:219], v199 offset:35840
	ds_read_b128 v[220:223], v199 offset:36864
	ds_read_b128 v[224:227], v199 offset:37888
	ds_read_b128 v[228:231], v199 offset:38912
	ds_read_b128 v[232:235], v199 offset:39936
	v_cndmask_b32_e32 v170, v178, v200, vcc
	global_load_lds_dwordx4 v168, s[48:49]
	s_mov_b32 m0, s60
	s_nop 0
	global_load_lds_dwordx4 v170, s[48:49]
	s_waitcnt vmcnt(8)
	s_waitcnt lgkmcnt(0)
	s_barrier
	s_setprio 1
	s_waitcnt lgkmcnt(0)
	v_mfma_f32_16x16x128_f8f6f4 v[158:161], v[2:9], v[204:211], v[158:161]
	v_mfma_f32_16x16x128_f8f6f4 v[150:153], v[10:17], v[204:211], v[150:153]
	v_mfma_f32_16x16x128_f8f6f4 v[142:145], v[2:9], v[212:219], v[142:145]
	v_mfma_f32_16x16x128_f8f6f4 v[134:137], v[10:17], v[212:219], v[134:137]
	v_mfma_f32_16x16x128_f8f6f4 v[126:129], v[2:9], v[220:227], v[126:129]
	v_mfma_f32_16x16x128_f8f6f4 v[118:121], v[10:17], v[220:227], v[118:121]
	v_mfma_f32_16x16x128_f8f6f4 v[110:113], v[2:9], v[228:235], v[110:113]
	v_mfma_f32_16x16x128_f8f6f4 v[102:105], v[10:17], v[228:235], v[102:105]
	s_setprio 0
	s_setprio 1
	v_mfma_f32_16x16x128_f8f6f4 v[154:157], v[18:25], v[204:211], v[154:157]
	v_mfma_f32_16x16x128_f8f6f4 v[146:149], v[26:33], v[204:211], v[146:149]
	v_mfma_f32_16x16x128_f8f6f4 v[138:141], v[18:25], v[212:219], v[138:141]
	v_mfma_f32_16x16x128_f8f6f4 v[130:133], v[26:33], v[212:219], v[130:133]
	v_mfma_f32_16x16x128_f8f6f4 v[122:125], v[18:25], v[220:227], v[122:125]
	v_mfma_f32_16x16x128_f8f6f4 v[114:117], v[26:33], v[220:227], v[114:117]
	v_mfma_f32_16x16x128_f8f6f4 v[106:109], v[18:25], v[228:235], v[106:109]
	v_mfma_f32_16x16x128_f8f6f4 v[98:101], v[26:33], v[228:235], v[98:101]
	s_setprio 0
	s_barrier
	s_add_i32 s46, s46, s52
	s_mov_b32 m0, s46
	ds_read_b128 v[204:207], v199 offset:49152
	ds_read_b128 v[208:211], v199 offset:50176
	ds_read_b128 v[212:215], v199 offset:51200
	ds_read_b128 v[216:219], v199 offset:52224
	ds_read_b128 v[220:223], v199 offset:53248
	ds_read_b128 v[224:227], v199 offset:54272
	ds_read_b128 v[228:231], v199 offset:55296
	ds_read_b128 v[232:235], v199 offset:56320
	s_add_u32 s98, s98, 0x80
	s_addc_u32 s99, s99, 0
	global_load_lds_dwordx4 v164, s[98:99]
	s_add_i32 m0, s46, 0x2000
	s_add_u32 s44, s44, 0x20080
	s_addc_u32 s45, s45, 0
	s_add_i32 s46, s47, s52
	global_load_lds_dwordx4 v166, s[98:99]
	s_mov_b32 m0, s46
	s_nop 0
	global_load_lds_dwordx4 v164, s[44:45]
	s_add_i32 m0, s46, 0x2000
	s_nop 0
	global_load_lds_dwordx4 v166, s[44:45]
	v_lshl_add_u64 v[184:185], v[190:191], 0, s[16:17]
	s_mov_b32 m0, s63
	s_nop 0
	global_load_lds_dwordx4 v[184:185], off
	v_lshl_add_u64 v[184:185], v[188:189], 0, s[16:17]
	s_mov_b32 m0, s64
	s_nop 0
	global_load_lds_dwordx4 v[184:185], off
	s_waitcnt vmcnt(8)
	s_waitcnt lgkmcnt(0)
	s_barrier
	s_setprio 1
	s_waitcnt lgkmcnt(0)
	v_mfma_f32_16x16x128_f8f6f4 v[94:97], v[2:9], v[204:211], v[94:97]
	v_mfma_f32_16x16x128_f8f6f4 v[86:89], v[10:17], v[204:211], v[86:89]
	v_mfma_f32_16x16x128_f8f6f4 v[78:81], v[2:9], v[212:219], v[78:81]
	v_mfma_f32_16x16x128_f8f6f4 v[70:73], v[10:17], v[212:219], v[70:73]
	v_mfma_f32_16x16x128_f8f6f4 v[58:61], v[2:9], v[220:227], v[58:61]
	v_mfma_f32_16x16x128_f8f6f4 v[46:49], v[10:17], v[220:227], v[46:49]
	v_mfma_f32_16x16x128_f8f6f4 v[38:41], v[2:9], v[228:235], v[38:41]
	v_mfma_f32_16x16x128_f8f6f4 v[34:37], v[10:17], v[228:235], v[34:37]
	s_setprio 0
	s_setprio 1
	v_mfma_f32_16x16x128_f8f6f4 v[90:93], v[18:25], v[204:211], v[90:93]
	v_mfma_f32_16x16x128_f8f6f4 v[82:85], v[26:33], v[204:211], v[82:85]
	v_mfma_f32_16x16x128_f8f6f4 v[74:77], v[18:25], v[212:219], v[74:77]
	v_mfma_f32_16x16x128_f8f6f4 v[66:69], v[26:33], v[212:219], v[66:69]
	v_mfma_f32_16x16x128_f8f6f4 v[50:53], v[18:25], v[220:227], v[50:53]
	v_mfma_f32_16x16x128_f8f6f4 v[42:45], v[26:33], v[220:227], v[42:45]
	v_mfma_f32_16x16x128_f8f6f4 v[62:65], v[18:25], v[228:235], v[62:65]
	v_mfma_f32_16x16x128_f8f6f4 v[54:57], v[26:33], v[228:235], v[54:57]
	s_setprio 0
	s_barrier
	s_add_i32 s79, s79, 2
	s_cmp_gt_u32 s79, 5
	s_mov_b64 s[46:47], s[42:43]
	s_cbranch_scc0 .LBB0_1911
	s_and_b64 vcc, exec, s[20:21]
	s_cbranch_vccz .LBB0_1914
	s_barrier
